# csr gather: nodes ordered by ceil(deg/4), 8-row passes plus one 4-row tail pass
# baseline (speedup 1.0000x reference)
.Lg4_start:
	v_lshl_or_b32 v60, v38, 4, v44
	v_lshlrev_b32_e32 v63, 2, v38
	v_sub_u32_e32 v57, v45, v63
	v_cmp_gt_u32_e32 vcc, 64, v60
	s_and_saveexec_b64 s[8:9], vcc
	s_cbranch_execz .Lg4_perm_done
	v_lshl_add_u32 v56, v60, 2, v57
	ds_read2_b32 v[58:59], v56 offset1:1
	s_waitcnt lgkmcnt(0)
	v_sub_u32_e32 v58, v59, v58
	v_add_u32_e32 v58, 3, v58
	v_lshrrev_b32_e32 v58, 2, v58
	v_min_u32_e32 v58, 15, v58
	v_mov_b32_e32 v59, 0
	s_mov_b32 s12, 0
	v_cmp_eq_u32_e64 s[46:47], 15, v58
	s_nop 1
	v_mbcnt_lo_u32_b32 v56, s46, 0
	v_mbcnt_hi_u32_b32 v56, s47, v56
	v_add_u32_e32 v56, s12, v56
	v_cndmask_b32_e64 v59, v59, v56, s[46:47]
	s_bcnt1_i32_b64 s13, s[46:47]
	s_add_i32 s12, s12, s13
	v_cmp_eq_u32_e64 s[48:49], 14, v58
	s_nop 1
	v_mbcnt_lo_u32_b32 v56, s48, 0
	v_mbcnt_hi_u32_b32 v56, s49, v56
	v_add_u32_e32 v56, s12, v56
	v_cndmask_b32_e64 v59, v59, v56, s[48:49]
	s_bcnt1_i32_b64 s13, s[48:49]
	s_add_i32 s12, s12, s13
	v_cmp_eq_u32_e64 s[46:47], 13, v58
	s_nop 1
	v_mbcnt_lo_u32_b32 v56, s46, 0
	v_mbcnt_hi_u32_b32 v56, s47, v56
	v_add_u32_e32 v56, s12, v56
	v_cndmask_b32_e64 v59, v59, v56, s[46:47]
	s_bcnt1_i32_b64 s13, s[46:47]
	s_add_i32 s12, s12, s13
	v_cmp_eq_u32_e64 s[48:49], 12, v58
	s_nop 1
	v_mbcnt_lo_u32_b32 v56, s48, 0
	v_mbcnt_hi_u32_b32 v56, s49, v56
	v_add_u32_e32 v56, s12, v56
	v_cndmask_b32_e64 v59, v59, v56, s[48:49]
	s_bcnt1_i32_b64 s13, s[48:49]
	s_add_i32 s12, s12, s13
	v_cmp_eq_u32_e64 s[46:47], 11, v58
	s_nop 1
	v_mbcnt_lo_u32_b32 v56, s46, 0
	v_mbcnt_hi_u32_b32 v56, s47, v56
	v_add_u32_e32 v56, s12, v56
	v_cndmask_b32_e64 v59, v59, v56, s[46:47]
	s_bcnt1_i32_b64 s13, s[46:47]
	s_add_i32 s12, s12, s13
	v_cmp_eq_u32_e64 s[48:49], 10, v58
	s_nop 1
	v_mbcnt_lo_u32_b32 v56, s48, 0
	v_mbcnt_hi_u32_b32 v56, s49, v56
	v_add_u32_e32 v56, s12, v56
	v_cndmask_b32_e64 v59, v59, v56, s[48:49]
	s_bcnt1_i32_b64 s13, s[48:49]
	s_add_i32 s12, s12, s13
	v_cmp_eq_u32_e64 s[46:47], 9, v58
	s_nop 1
	v_mbcnt_lo_u32_b32 v56, s46, 0
	v_mbcnt_hi_u32_b32 v56, s47, v56
	v_add_u32_e32 v56, s12, v56
	v_cndmask_b32_e64 v59, v59, v56, s[46:47]
	s_bcnt1_i32_b64 s13, s[46:47]
	s_add_i32 s12, s12, s13
	v_cmp_eq_u32_e64 s[48:49], 8, v58
	s_nop 1
	v_mbcnt_lo_u32_b32 v56, s48, 0
	v_mbcnt_hi_u32_b32 v56, s49, v56
	v_add_u32_e32 v56, s12, v56
	v_cndmask_b32_e64 v59, v59, v56, s[48:49]
	s_bcnt1_i32_b64 s13, s[48:49]
	s_add_i32 s12, s12, s13
	v_cmp_eq_u32_e64 s[46:47], 7, v58
	s_nop 1
	v_mbcnt_lo_u32_b32 v56, s46, 0
	v_mbcnt_hi_u32_b32 v56, s47, v56
	v_add_u32_e32 v56, s12, v56
	v_cndmask_b32_e64 v59, v59, v56, s[46:47]
	s_bcnt1_i32_b64 s13, s[46:47]
	s_add_i32 s12, s12, s13
	v_cmp_eq_u32_e64 s[48:49], 6, v58
	s_nop 1
	v_mbcnt_lo_u32_b32 v56, s48, 0
	v_mbcnt_hi_u32_b32 v56, s49, v56
	v_add_u32_e32 v56, s12, v56
	v_cndmask_b32_e64 v59, v59, v56, s[48:49]
	s_bcnt1_i32_b64 s13, s[48:49]
	s_add_i32 s12, s12, s13
	v_cmp_eq_u32_e64 s[46:47], 5, v58
	s_nop 1
	v_mbcnt_lo_u32_b32 v56, s46, 0
	v_mbcnt_hi_u32_b32 v56, s47, v56
	v_add_u32_e32 v56, s12, v56
	v_cndmask_b32_e64 v59, v59, v56, s[46:47]
	s_bcnt1_i32_b64 s13, s[46:47]
	s_add_i32 s12, s12, s13
	v_cmp_eq_u32_e64 s[48:49], 4, v58
	s_nop 1
	v_mbcnt_lo_u32_b32 v56, s48, 0
	v_mbcnt_hi_u32_b32 v56, s49, v56
	v_add_u32_e32 v56, s12, v56
	v_cndmask_b32_e64 v59, v59, v56, s[48:49]
	s_bcnt1_i32_b64 s13, s[48:49]
	s_add_i32 s12, s12, s13
	v_cmp_eq_u32_e64 s[46:47], 3, v58
	s_nop 1
	v_mbcnt_lo_u32_b32 v56, s46, 0
	v_mbcnt_hi_u32_b32 v56, s47, v56
	v_add_u32_e32 v56, s12, v56
	v_cndmask_b32_e64 v59, v59, v56, s[46:47]
	s_bcnt1_i32_b64 s13, s[46:47]
	s_add_i32 s12, s12, s13
	v_cmp_eq_u32_e64 s[48:49], 2, v58
	s_nop 1
	v_mbcnt_lo_u32_b32 v56, s48, 0
	v_mbcnt_hi_u32_b32 v56, s49, v56
	v_add_u32_e32 v56, s12, v56
	v_cndmask_b32_e64 v59, v59, v56, s[48:49]
	s_bcnt1_i32_b64 s13, s[48:49]
	s_add_i32 s12, s12, s13
	v_cmp_eq_u32_e64 s[46:47], 1, v58
	s_nop 1
	v_mbcnt_lo_u32_b32 v56, s46, 0
	v_mbcnt_hi_u32_b32 v56, s47, v56
	v_add_u32_e32 v56, s12, v56
	v_cndmask_b32_e64 v59, v59, v56, s[46:47]
	s_bcnt1_i32_b64 s13, s[46:47]
	s_add_i32 s12, s12, s13
	v_cmp_eq_u32_e64 s[48:49], 0, v58
	s_nop 1
	v_mbcnt_lo_u32_b32 v56, s48, 0
	v_mbcnt_hi_u32_b32 v56, s49, v56
	v_add_u32_e32 v56, s12, v56
	v_cndmask_b32_e64 v59, v59, v56, s[48:49]
	s_bcnt1_i32_b64 s13, s[48:49]
	s_add_i32 s12, s12, s13
	v_lshlrev_b32_e32 v56, 2, v59
	ds_write_b32 v56, v60

.Lg4_loop:
	s_add_i32 s12, s15, 4
	v_cmp_lt_i32_e32 vcc, s12, v59
	s_and_b64 vcc, exec, vcc
	s_cbranch_vccz .Lg4_half
	ds_read_u16 v48, v58
	ds_read_u16 v49, v58 offset:2
	ds_read_u16 v50, v58 offset:4
	ds_read_u16 v51, v58 offset:6
	ds_read_u16 v52, v58 offset:8
	ds_read_u16 v53, v58 offset:10
	ds_read_u16 v54, v58 offset:12
	ds_read_u16 v55, v58 offset:14
	s_add_i32 s12, s15, 1
	v_cmp_lt_i32_e64 s[46:47], s12, v59
	s_add_i32 s12, s15, 2
	v_cmp_lt_i32_e64 s[48:49], s12, v59
	s_add_i32 s12, s15, 3
	v_cmp_lt_i32_e64 s[50:51], s12, v59
	s_add_i32 s12, s15, 4
	v_cmp_lt_i32_e64 s[52:53], s12, v59
	s_add_i32 s12, s15, 5
	v_cmp_lt_i32_e64 s[54:55], s12, v59
	s_add_i32 s12, s15, 6
	v_cmp_lt_i32_e64 s[56:57], s12, v59
	s_add_i32 s12, s15, 7
	v_cmp_lt_i32_e64 s[58:59], s12, v59
	s_waitcnt lgkmcnt(7)
	v_lshl_or_b32 v48, v48, 7, v61
	global_load_dwordx4 v[16:19], v48, s[34:35]
	s_waitcnt lgkmcnt(6)
	v_cndmask_b32_e64 v49, v63, v49, s[46:47]
	v_lshl_or_b32 v49, v49, 7, v61
	global_load_dwordx4 v[20:23], v49, s[34:35]
	s_waitcnt lgkmcnt(5)
	v_cndmask_b32_e64 v50, v63, v50, s[48:49]
	v_lshl_or_b32 v50, v50, 7, v61
	global_load_dwordx4 v[24:27], v50, s[34:35]
	s_waitcnt lgkmcnt(4)
	v_cndmask_b32_e64 v51, v63, v51, s[50:51]
	v_lshl_or_b32 v51, v51, 7, v61
	global_load_dwordx4 v[28:31], v51, s[34:35]
	s_waitcnt lgkmcnt(3)
	v_cndmask_b32_e64 v52, v63, v52, s[52:53]
	v_lshl_or_b32 v52, v52, 7, v61
	global_load_dwordx4 v[32:35], v52, s[34:35]
	s_waitcnt lgkmcnt(2)
	v_cndmask_b32_e64 v53, v63, v53, s[54:55]
	v_lshl_or_b32 v53, v53, 7, v61
	global_load_dwordx4 v[36:39], v53, s[34:35]
	s_waitcnt lgkmcnt(1)
	v_cndmask_b32_e64 v54, v63, v54, s[56:57]
	v_lshl_or_b32 v54, v54, 7, v61
	global_load_dwordx4 v[40:43], v54, s[34:35]
	s_waitcnt lgkmcnt(0)
	v_cndmask_b32_e64 v55, v63, v55, s[58:59]
	v_lshl_or_b32 v55, v55, 7, v61
	global_load_dwordx4 v[44:47], v55, s[34:35]
	s_waitcnt vmcnt(7)
	v_cvt_pk_f32_fp8_e32 v[48:49], v16
	v_cvt_pk_f32_fp8_sdwa v[50:51], v16 src0_sel:WORD_1
	v_pk_add_f32 v[0:1], v[0:1], v[48:49]
	v_pk_add_f32 v[2:3], v[2:3], v[50:51]
	v_cvt_pk_f32_fp8_e32 v[52:53], v17
	v_cvt_pk_f32_fp8_sdwa v[54:55], v17 src0_sel:WORD_1
	v_pk_add_f32 v[4:5], v[4:5], v[52:53]
	v_pk_add_f32 v[6:7], v[6:7], v[54:55]
	v_cvt_pk_f32_fp8_e32 v[48:49], v18
	v_cvt_pk_f32_fp8_sdwa v[50:51], v18 src0_sel:WORD_1
	v_pk_add_f32 v[8:9], v[8:9], v[48:49]
	v_pk_add_f32 v[10:11], v[10:11], v[50:51]
	v_cvt_pk_f32_fp8_e32 v[52:53], v19
	v_cvt_pk_f32_fp8_sdwa v[54:55], v19 src0_sel:WORD_1
	v_pk_add_f32 v[12:13], v[12:13], v[52:53]
	v_pk_add_f32 v[14:15], v[14:15], v[54:55]
	s_waitcnt vmcnt(6)
	v_cvt_pk_f32_fp8_e32 v[48:49], v20
	v_cvt_pk_f32_fp8_sdwa v[50:51], v20 src0_sel:WORD_1
	v_pk_add_f32 v[0:1], v[0:1], v[48:49]
	v_pk_add_f32 v[2:3], v[2:3], v[50:51]
	v_cvt_pk_f32_fp8_e32 v[52:53], v21
	v_cvt_pk_f32_fp8_sdwa v[54:55], v21 src0_sel:WORD_1
	v_pk_add_f32 v[4:5], v[4:5], v[52:53]
	v_pk_add_f32 v[6:7], v[6:7], v[54:55]
	v_cvt_pk_f32_fp8_e32 v[48:49], v22
	v_cvt_pk_f32_fp8_sdwa v[50:51], v22 src0_sel:WORD_1
	v_pk_add_f32 v[8:9], v[8:9], v[48:49]
	v_pk_add_f32 v[10:11], v[10:11], v[50:51]
	v_cvt_pk_f32_fp8_e32 v[52:53], v23
	v_cvt_pk_f32_fp8_sdwa v[54:55], v23 src0_sel:WORD_1
	v_pk_add_f32 v[12:13], v[12:13], v[52:53]
	v_pk_add_f32 v[14:15], v[14:15], v[54:55]
	s_waitcnt vmcnt(5)
	v_cvt_pk_f32_fp8_e32 v[48:49], v24
	v_cvt_pk_f32_fp8_sdwa v[50:51], v24 src0_sel:WORD_1
	v_pk_add_f32 v[0:1], v[0:1], v[48:49]
	v_pk_add_f32 v[2:3], v[2:3], v[50:51]
	v_cvt_pk_f32_fp8_e32 v[52:53], v25
	v_cvt_pk_f32_fp8_sdwa v[54:55], v25 src0_sel:WORD_1
	v_pk_add_f32 v[4:5], v[4:5], v[52:53]
	v_pk_add_f32 v[6:7], v[6:7], v[54:55]
	v_cvt_pk_f32_fp8_e32 v[48:49], v26
	v_cvt_pk_f32_fp8_sdwa v[50:51], v26 src0_sel:WORD_1
	v_pk_add_f32 v[8:9], v[8:9], v[48:49]
	v_pk_add_f32 v[10:11], v[10:11], v[50:51]
	v_cvt_pk_f32_fp8_e32 v[52:53], v27
	v_cvt_pk_f32_fp8_sdwa v[54:55], v27 src0_sel:WORD_1
	v_pk_add_f32 v[12:13], v[12:13], v[52:53]
	v_pk_add_f32 v[14:15], v[14:15], v[54:55]
	s_waitcnt vmcnt(4)
	v_cvt_pk_f32_fp8_e32 v[48:49], v28
	v_cvt_pk_f32_fp8_sdwa v[50:51], v28 src0_sel:WORD_1
	v_pk_add_f32 v[0:1], v[0:1], v[48:49]
	v_pk_add_f32 v[2:3], v[2:3], v[50:51]
	v_cvt_pk_f32_fp8_e32 v[52:53], v29
	v_cvt_pk_f32_fp8_sdwa v[54:55], v29 src0_sel:WORD_1
	v_pk_add_f32 v[4:5], v[4:5], v[52:53]
	v_pk_add_f32 v[6:7], v[6:7], v[54:55]
	v_cvt_pk_f32_fp8_e32 v[48:49], v30
	v_cvt_pk_f32_fp8_sdwa v[50:51], v30 src0_sel:WORD_1
	v_pk_add_f32 v[8:9], v[8:9], v[48:49]
	v_pk_add_f32 v[10:11], v[10:11], v[50:51]
	v_cvt_pk_f32_fp8_e32 v[52:53], v31
	v_cvt_pk_f32_fp8_sdwa v[54:55], v31 src0_sel:WORD_1
	v_pk_add_f32 v[12:13], v[12:13], v[52:53]
	v_pk_add_f32 v[14:15], v[14:15], v[54:55]
	s_waitcnt vmcnt(3)
	v_cvt_pk_f32_fp8_e32 v[48:49], v32
	v_cvt_pk_f32_fp8_sdwa v[50:51], v32 src0_sel:WORD_1
	v_pk_add_f32 v[0:1], v[0:1], v[48:49]
	v_pk_add_f32 v[2:3], v[2:3], v[50:51]
	v_cvt_pk_f32_fp8_e32 v[52:53], v33
	v_cvt_pk_f32_fp8_sdwa v[54:55], v33 src0_sel:WORD_1
	v_pk_add_f32 v[4:5], v[4:5], v[52:53]
	v_pk_add_f32 v[6:7], v[6:7], v[54:55]
	v_cvt_pk_f32_fp8_e32 v[48:49], v34
	v_cvt_pk_f32_fp8_sdwa v[50:51], v34 src0_sel:WORD_1
	v_pk_add_f32 v[8:9], v[8:9], v[48:49]
	v_pk_add_f32 v[10:11], v[10:11], v[50:51]
	v_cvt_pk_f32_fp8_e32 v[52:53], v35
	v_cvt_pk_f32_fp8_sdwa v[54:55], v35 src0_sel:WORD_1
	v_pk_add_f32 v[12:13], v[12:13], v[52:53]
	v_pk_add_f32 v[14:15], v[14:15], v[54:55]
	s_waitcnt vmcnt(2)
	v_cvt_pk_f32_fp8_e32 v[48:49], v36
	v_cvt_pk_f32_fp8_sdwa v[50:51], v36 src0_sel:WORD_1
	v_pk_add_f32 v[0:1], v[0:1], v[48:49]
	v_pk_add_f32 v[2:3], v[2:3], v[50:51]
	v_cvt_pk_f32_fp8_e32 v[52:53], v37
	v_cvt_pk_f32_fp8_sdwa v[54:55], v37 src0_sel:WORD_1
	v_pk_add_f32 v[4:5], v[4:5], v[52:53]
	v_pk_add_f32 v[6:7], v[6:7], v[54:55]
	v_cvt_pk_f32_fp8_e32 v[48:49], v38
	v_cvt_pk_f32_fp8_sdwa v[50:51], v38 src0_sel:WORD_1
	v_pk_add_f32 v[8:9], v[8:9], v[48:49]
	v_pk_add_f32 v[10:11], v[10:11], v[50:51]
	v_cvt_pk_f32_fp8_e32 v[52:53], v39
	v_cvt_pk_f32_fp8_sdwa v[54:55], v39 src0_sel:WORD_1
	v_pk_add_f32 v[12:13], v[12:13], v[52:53]
	v_pk_add_f32 v[14:15], v[14:15], v[54:55]
	s_waitcnt vmcnt(1)
	v_cvt_pk_f32_fp8_e32 v[48:49], v40
	v_cvt_pk_f32_fp8_sdwa v[50:51], v40 src0_sel:WORD_1
	v_pk_add_f32 v[0:1], v[0:1], v[48:49]
	v_pk_add_f32 v[2:3], v[2:3], v[50:51]
	v_cvt_pk_f32_fp8_e32 v[52:53], v41
	v_cvt_pk_f32_fp8_sdwa v[54:55], v41 src0_sel:WORD_1
	v_pk_add_f32 v[4:5], v[4:5], v[52:53]
	v_pk_add_f32 v[6:7], v[6:7], v[54:55]
	v_cvt_pk_f32_fp8_e32 v[48:49], v42
	v_cvt_pk_f32_fp8_sdwa v[50:51], v42 src0_sel:WORD_1
	v_pk_add_f32 v[8:9], v[8:9], v[48:49]
	v_pk_add_f32 v[10:11], v[10:11], v[50:51]
	v_cvt_pk_f32_fp8_e32 v[52:53], v43
	v_cvt_pk_f32_fp8_sdwa v[54:55], v43 src0_sel:WORD_1
	v_pk_add_f32 v[12:13], v[12:13], v[52:53]
	v_pk_add_f32 v[14:15], v[14:15], v[54:55]
	s_waitcnt vmcnt(0)
	v_cvt_pk_f32_fp8_e32 v[48:49], v44
	v_cvt_pk_f32_fp8_sdwa v[50:51], v44 src0_sel:WORD_1
	v_pk_add_f32 v[0:1], v[0:1], v[48:49]
	v_pk_add_f32 v[2:3], v[2:3], v[50:51]
	v_cvt_pk_f32_fp8_e32 v[52:53], v45
	v_cvt_pk_f32_fp8_sdwa v[54:55], v45 src0_sel:WORD_1
	v_pk_add_f32 v[4:5], v[4:5], v[52:53]
	v_pk_add_f32 v[6:7], v[6:7], v[54:55]
	v_cvt_pk_f32_fp8_e32 v[48:49], v46
	v_cvt_pk_f32_fp8_sdwa v[50:51], v46 src0_sel:WORD_1
	v_pk_add_f32 v[8:9], v[8:9], v[48:49]
	v_pk_add_f32 v[10:11], v[10:11], v[50:51]
	v_cvt_pk_f32_fp8_e32 v[52:53], v47
	v_cvt_pk_f32_fp8_sdwa v[54:55], v47 src0_sel:WORD_1
	v_pk_add_f32 v[12:13], v[12:13], v[52:53]
	v_pk_add_f32 v[14:15], v[14:15], v[54:55]
	s_add_i32 s15, s15, 8
	v_cmp_ge_i32_e32 vcc, s15, v59
	v_add_u32_e32 v58, 16, v58
	s_or_b64 s[2:3], vcc, s[2:3]
	s_andn2_b64 exec, exec, s[2:3]
	s_cbranch_execnz .Lg4_loop
	s_branch .Lg4_loop_skip
.Lg4_half:
	ds_read_u16 v48, v58
	ds_read_u16 v49, v58 offset:2
	ds_read_u16 v50, v58 offset:4
	ds_read_u16 v51, v58 offset:6
	s_add_i32 s12, s15, 1
	v_cmp_lt_i32_e64 s[46:47], s12, v59
	s_add_i32 s12, s15, 2
	v_cmp_lt_i32_e64 s[48:49], s12, v59
	s_add_i32 s12, s15, 3
	v_cmp_lt_i32_e64 s[50:51], s12, v59
	s_waitcnt lgkmcnt(3)
	v_lshl_or_b32 v48, v48, 7, v61
	global_load_dwordx4 v[16:19], v48, s[34:35]
	s_waitcnt lgkmcnt(2)
	v_cndmask_b32_e64 v49, v63, v49, s[46:47]
	v_lshl_or_b32 v49, v49, 7, v61
	global_load_dwordx4 v[20:23], v49, s[34:35]
	s_waitcnt lgkmcnt(1)
	v_cndmask_b32_e64 v50, v63, v50, s[48:49]
	v_lshl_or_b32 v50, v50, 7, v61
	global_load_dwordx4 v[24:27], v50, s[34:35]
	s_waitcnt lgkmcnt(0)
	v_cndmask_b32_e64 v51, v63, v51, s[50:51]
	v_lshl_or_b32 v51, v51, 7, v61
	global_load_dwordx4 v[28:31], v51, s[34:35]
	s_nop 0
	s_waitcnt vmcnt(3)
	v_cvt_pk_f32_fp8_e32 v[52:53], v16
	v_cvt_pk_f32_fp8_sdwa v[54:55], v16 src0_sel:WORD_1
	v_pk_add_f32 v[0:1], v[0:1], v[52:53]
	v_pk_add_f32 v[2:3], v[2:3], v[54:55]
	v_cvt_pk_f32_fp8_e32 v[52:53], v17
	v_cvt_pk_f32_fp8_sdwa v[54:55], v17 src0_sel:WORD_1
	v_pk_add_f32 v[4:5], v[4:5], v[52:53]
	v_pk_add_f32 v[6:7], v[6:7], v[54:55]
	v_cvt_pk_f32_fp8_e32 v[52:53], v18
	v_cvt_pk_f32_fp8_sdwa v[54:55], v18 src0_sel:WORD_1
	v_pk_add_f32 v[8:9], v[8:9], v[52:53]
	v_pk_add_f32 v[10:11], v[10:11], v[54:55]
	v_cvt_pk_f32_fp8_e32 v[52:53], v19
	v_cvt_pk_f32_fp8_sdwa v[54:55], v19 src0_sel:WORD_1
	v_pk_add_f32 v[12:13], v[12:13], v[52:53]
	v_pk_add_f32 v[14:15], v[14:15], v[54:55]
	s_waitcnt vmcnt(2)
	v_cvt_pk_f32_fp8_e32 v[52:53], v20
	v_cvt_pk_f32_fp8_sdwa v[54:55], v20 src0_sel:WORD_1
	v_pk_add_f32 v[0:1], v[0:1], v[52:53]
	v_pk_add_f32 v[2:3], v[2:3], v[54:55]
	v_cvt_pk_f32_fp8_e32 v[52:53], v21
	v_cvt_pk_f32_fp8_sdwa v[54:55], v21 src0_sel:WORD_1
	v_pk_add_f32 v[4:5], v[4:5], v[52:53]
	v_pk_add_f32 v[6:7], v[6:7], v[54:55]
	v_cvt_pk_f32_fp8_e32 v[52:53], v22
	v_cvt_pk_f32_fp8_sdwa v[54:55], v22 src0_sel:WORD_1
	v_pk_add_f32 v[8:9], v[8:9], v[52:53]
	v_pk_add_f32 v[10:11], v[10:11], v[54:55]
	v_cvt_pk_f32_fp8_e32 v[52:53], v23
	v_cvt_pk_f32_fp8_sdwa v[54:55], v23 src0_sel:WORD_1
	v_pk_add_f32 v[12:13], v[12:13], v[52:53]
	v_pk_add_f32 v[14:15], v[14:15], v[54:55]
	s_waitcnt vmcnt(1)
	v_cvt_pk_f32_fp8_e32 v[52:53], v24
	v_cvt_pk_f32_fp8_sdwa v[54:55], v24 src0_sel:WORD_1
	v_pk_add_f32 v[0:1], v[0:1], v[52:53]
	v_pk_add_f32 v[2:3], v[2:3], v[54:55]
	v_cvt_pk_f32_fp8_e32 v[52:53], v25
	v_cvt_pk_f32_fp8_sdwa v[54:55], v25 src0_sel:WORD_1
	v_pk_add_f32 v[4:5], v[4:5], v[52:53]
	v_pk_add_f32 v[6:7], v[6:7], v[54:55]
	v_cvt_pk_f32_fp8_e32 v[52:53], v26
	v_cvt_pk_f32_fp8_sdwa v[54:55], v26 src0_sel:WORD_1
	v_pk_add_f32 v[8:9], v[8:9], v[52:53]
	v_pk_add_f32 v[10:11], v[10:11], v[54:55]
	v_cvt_pk_f32_fp8_e32 v[52:53], v27
	v_cvt_pk_f32_fp8_sdwa v[54:55], v27 src0_sel:WORD_1
	v_pk_add_f32 v[12:13], v[12:13], v[52:53]
	v_pk_add_f32 v[14:15], v[14:15], v[54:55]
	s_waitcnt vmcnt(0)
	v_cvt_pk_f32_fp8_e32 v[52:53], v28
	v_cvt_pk_f32_fp8_sdwa v[54:55], v28 src0_sel:WORD_1
	v_pk_add_f32 v[0:1], v[0:1], v[52:53]
	v_pk_add_f32 v[2:3], v[2:3], v[54:55]
	v_cvt_pk_f32_fp8_e32 v[52:53], v29
	v_cvt_pk_f32_fp8_sdwa v[54:55], v29 src0_sel:WORD_1
	v_pk_add_f32 v[4:5], v[4:5], v[52:53]
	v_pk_add_f32 v[6:7], v[6:7], v[54:55]
	v_cvt_pk_f32_fp8_e32 v[52:53], v30
	v_cvt_pk_f32_fp8_sdwa v[54:55], v30 src0_sel:WORD_1
	v_pk_add_f32 v[8:9], v[8:9], v[52:53]
	v_pk_add_f32 v[10:11], v[10:11], v[54:55]
	v_cvt_pk_f32_fp8_e32 v[52:53], v31
	v_cvt_pk_f32_fp8_sdwa v[54:55], v31 src0_sel:WORD_1
	v_pk_add_f32 v[12:13], v[12:13], v[52:53]
	v_pk_add_f32 v[14:15], v[14:15], v[54:55]
